# quota 3 plus before-attention converters additionally stop at the midpoint of the remaining queue range
# speedup vs baseline: 1.0193x; 1.0193x over previous
; __device__ __forceinline__ unsigned xb_add(unsigned* p, unsigned v) { return __hip_atomic_fetch_add(p, v, __ATOMIC_RELAXED, __HIP_MEMORY_SCOPE_AGENT); }
;     ...
;     for (int nc = 0; nc < max_claims; ++nc) {
;         if (tl == 0) { st[6] = ahead; if (ahead < (unsigned)target && nc + 1 < max_claims) ahead = (ahead + 32u < (unsigned)target) ? xb_add(qw, 32u) : 0xFFFFFFFFu; }
;         __syncthreads();
.LBB0_698:
	s_and_saveexec_b64 s[0:1], s[2:3]
	s_cbranch_execz .LBB0_706
	v_readlane_b32 s14, v254, 27
	s_cmp_lt_u32 s30, 2
	v_cmp_gt_u32_e32 vcc, s101, v129
	v_mov_b32_e32 v139, s14
	s_cselect_b64 s[14:15], -1, 0
	s_and_b64 s[16:17], vcc, s[14:15]
	ds_write_b32 v139, v129
	s_nop 1
	v_mov_b32_e32 v129, -1
	s_and_saveexec_b64 s[14:15], s[16:17]
	s_cbranch_execz .LBB0_705
	s_mov_b64 vcc, exec
	v_mov_b32_e32 v129, -1
	s_and_saveexec_b64 s[16:17], vcc
	s_cbranch_execz .LBB0_704
	s_mov_b64 s[20:21], exec
	v_mbcnt_lo_u32_b32 v129, s20, 0
	v_mbcnt_hi_u32_b32 v129, s21, v129
	v_cmp_eq_u32_e32 vcc, 0, v129
	s_and_saveexec_b64 s[18:19], vcc
	s_cbranch_execz .LBB0_703
	s_bcnt1_i32_b64 s20, s[20:21]
	s_lshl_b32 s20, s20, 5
	v_mov_b32_e32 v139, s20
	global_atomic_add v139, v193, v139, s[4:5] sc0
